# P7 batch loop: next batch's 16 row loads prefetched into dead stage-B registers after stage B, copied at the next loop top; router-bias load hoisted in front of them
# speedup vs baseline: 1.0066x; 1.0066x over previous
; __device__ __forceinline__ f32x4 ld_bf4(const bf16_t* p) { const u32x2 w = *(const u32x2*)p; return (f32x4){__builtin_bit_cast(float, w.x << 16), __builtin_bit_cast(float, w.x & 0xffff0000u), __builtin_bit_cast(float, w.y << 16), __builtin_bit_cast(float, w.y & 0xffff0000u)}; }
; template <bool FAST>
; __device__ __forceinline__ void p7_route_t(Frame& F, const bool do_route) {
;     ...
;     for (int it = 0; it < NIT; ++it) {
;         const int row_ = FAST ? (F.bx * NIT + it) * 8 + F.wave : gw + it * NGW;
;         const bool valid = row_ < M_LAT; const int row = valid ? row_ : M_LAT - 1;
;         const float* mr = mod + (row / T) * NMOD;
;         f32x4 v[8], xv[8]; float ss = 0.f;
; #pragma unroll
;         for (int j = 0; j < 8; ++j) { v[j] = ld_bf4(MIX + (size_t)row * D + 4 * F.lane + 256 * j); xv[j] = *(const f32x4*)(IN_X + (size_t)row * D + 4 * F.lane + 256 * j); }
.LBB0_790:
	s_add_i32 s0, s93, s33
	s_lshl_b32 s0, s0, 3
	v_readlane_b32 s1, v254, 35
	s_add_i32 s90, s0, s1
	s_cmpk_gt_i32 s90, 0x3fff
	s_cselect_b64 s[0:1], -1, 0
	s_cmpk_lt_i32 s90, 0x4000
	s_cselect_b64 s[18:19], -1, 0
	s_min_i32 s16, s90, 0x3fff
	s_ashr_i32 s17, s16, 31
	s_lshl_b64 s[2:3], s[16:17], 12
	v_lshl_add_u64 v[2:3], v[36:37], 0, s[2:3]
	s_cmp_lg_u32 s33, 0
	s_cbranch_scc1 .Lp7_pref_copy
	global_load_dwordx2 v[30:31], v[2:3], off offset:1536
	global_load_dwordx2 v[44:45], v[2:3], off offset:3584
	global_load_dwordx2 v[50:51], v[2:3], off
	global_load_dwordx2 v[52:53], v[2:3], off offset:512
	global_load_dwordx2 v[54:55], v[2:3], off offset:1024
	global_load_dwordx2 v[56:57], v[2:3], off offset:2048
	global_load_dwordx2 v[58:59], v[2:3], off offset:2560
	global_load_dwordx2 v[110:111], v[2:3], off offset:3072
	s_lshl_b64 s[2:3], s[16:17], 13
	v_lshl_add_u64 v[2:3], v[38:39], 0, s[2:3]
	global_load_dwordx4 v[46:49], v[2:3], off
	global_load_dwordx4 v[26:29], v[2:3], off offset:1024
	global_load_dwordx4 v[22:25], v[2:3], off offset:2048
	global_load_dwordx4 v[18:21], v[2:3], off offset:3072
	v_add_co_u32_e32 v2, vcc, s92, v2
	s_ashr_i32 s91, s90, 31
	s_nop 0
	v_addc_co_u32_e32 v3, vcc, 0, v3, vcc
	global_load_dwordx4 v[14:17], v[2:3], off
	global_load_dwordx4 v[10:13], v[2:3], off offset:1024
	global_load_dwordx4 v[6:9], v[2:3], off offset:2048
	s_nop 0
	global_load_dwordx4 v[2:5], v[2:3], off offset:3072
	s_branch .Lp7_pref_go
.Lp7_pref_copy:
	s_lshl_b64 s[2:3], s[16:17], 13
	s_ashr_i32 s91, s90, 31
	s_waitcnt vmcnt(0)
	v_mov_b64_e32 v[30:31], v[122:123]
	v_mov_b64_e32 v[44:45], v[124:125]
	v_mov_b64_e32 v[50:51], v[126:127]
	v_mov_b64_e32 v[52:53], v[128:129]
	v_mov_b64_e32 v[54:55], v[130:131]
	v_mov_b64_e32 v[56:57], v[132:133]
	v_mov_b64_e32 v[58:59], v[134:135]
	v_mov_b64_e32 v[110:111], v[136:137]
	v_mov_b64_e32 v[46:47], v[138:139]
	v_mov_b64_e32 v[48:49], v[140:141]
	v_mov_b64_e32 v[26:27], v[142:143]
	v_mov_b64_e32 v[28:29], v[144:145]
	v_mov_b64_e32 v[22:23], v[146:147]
	v_mov_b64_e32 v[24:25], v[148:149]
	v_mov_b64_e32 v[18:19], v[150:151]
	v_mov_b64_e32 v[20:21], v[152:153]
	v_mov_b64_e32 v[14:15], v[154:155]
	v_mov_b64_e32 v[16:17], v[156:157]
	v_mov_b64_e32 v[10:11], v[158:159]
	v_mov_b64_e32 v[12:13], v[160:161]
	v_mov_b64_e32 v[6:7], v[162:163]
	v_mov_b64_e32 v[8:9], v[164:165]
	v_mov_b64_e32 v[2:3], v[166:167]
	v_mov_b64_e32 v[4:5], v[168:169]
; #define LAS __attribute__((address_space(3)))
; __device__ __forceinline__ f32x4 ld_bf4(const bf16_t* p) { const u32x2 w = *(const u32x2*)p; return (f32x4){__builtin_bit_cast(float, w.x << 16), __builtin_bit_cast(float, w.x & 0xffff0000u), __builtin_bit_cast(float, w.y << 16), __builtin_bit_cast(float, w.y & 0xffff0000u)}; }
; __device__ __forceinline__ void st_bf4(bf16_t* p, f32x4 v) { u32x2 w; w.x = pg8::cvt_pk_bf16(v.x, v.y); w.y = pg8::cvt_pk_bf16(v.z, v.w); *(u32x2*)p = w; }
; template <bool FAST>
; __device__ __forceinline__ void p7_route_t(Frame& F, const bool do_route) {
;     ...
;         for (int j = 0; j < 8; ++j) { v[j] = ld_bf4(MIX + (size_t)row * D + 4 * F.lane + 256 * j); xv[j] = *(const f32x4*)(IN_X + (size_t)row * D + 4 * F.lane + 256 * j); }
; #pragma unroll
;         for (int j = 0; j < 8; ++j) ss += (v[j].x * v[j].x + v[j].y * v[j].y) + (v[j].z * v[j].z + v[j].w * v[j].w);
;         float rstd = __builtin_amdgcn_rsqf(wave_sum(ss) * (1.0f / D) + RMS_EPS);
;         ss = 0.f;
; #pragma unroll
;         for (int j = 0; j < 8; ++j) { const int c = 4 * F.lane + 256 * j;
;             const f32x4 gg = FAST ? *(const LAS f32x4*)(pvec + c) : *(const f32x4*)(IN_NORMG + D + c) * *(const f32x4*)(mr + 2 * D + c);
;             v[j] = xv[j] + gg * (v[j] * rstd);
;             if (valid) st_bf4(X1 + (size_t)row * D + c, v[j]);
.Lp7_pref_go:
	s_waitcnt vmcnt(15)
	v_lshlrev_b32_e32 v63, 16, v30
	v_and_b32_e32 v61, 0xffff0000, v30
	s_waitcnt vmcnt(13)
	v_and_b32_e32 v115, 0xffff0000, v50
	v_and_b32_e32 v117, 0xffff0000, v51
	v_lshlrev_b32_e32 v64, 16, v31
	v_and_b32_e32 v65, 0xffff0000, v31
	v_lshlrev_b32_e32 v33, 16, v44
	v_and_b32_e32 v31, 0xffff0000, v44
	v_lshlrev_b32_e32 v114, 16, v50
	v_lshlrev_b32_e32 v116, 16, v51
	s_waitcnt vmcnt(12)
	v_and_b32_e32 v77, 0xffff0000, v53
	v_and_b32_e32 v76, 0xffff0000, v52
	s_waitcnt vmcnt(11)
	v_and_b32_e32 v73, 0xffff0000, v55
	v_mul_f32_e32 v30, v117, v117
	v_mul_f32_e32 v32, v115, v115
	v_lshlrev_b32_e32 v75, 16, v53
	v_lshlrev_b32_e32 v74, 16, v52
	v_lshlrev_b32_e32 v70, 16, v54
	v_and_b32_e32 v71, 0xffff0000, v54
	v_lshlrev_b32_e32 v72, 16, v55
	v_pk_mul_f32 v[54:55], v[76:77], v[76:77]
	v_mul_f32_e32 v62, v73, v73
	v_pk_fma_f32 v[120:121], v[116:117], v[116:117], v[30:31] op_sel_hi:[1,1,0]
	v_pk_fma_f32 v[122:123], v[114:115], v[114:115], v[32:33] op_sel_hi:[1,1,0]
	s_waitcnt vmcnt(8)
	v_lshlrev_b32_e32 v50, 16, v110
	v_and_b32_e32 v51, 0xffff0000, v110
	v_lshlrev_b32_e32 v52, 16, v111
	v_and_b32_e32 v53, 0xffff0000, v111
	v_mov_b32_e32 v111, v63
	v_mul_f32_e32 v60, v71, v71
	v_pk_fma_f32 v[54:55], v[74:75], v[74:75], v[54:55]
	v_pk_fma_f32 v[126:127], v[72:73], v[72:73], v[62:63] op_sel_hi:[1,1,0]
	v_mov_b32_e32 v62, v122
	v_mov_b32_e32 v110, v120
	v_mul_f32_e32 v128, v61, v61
	v_mul_f32_e32 v129, v64, v64
	v_mul_f32_e32 v130, v65, v65
	v_pk_fma_f32 v[124:125], v[70:71], v[70:71], v[60:61] op_sel_hi:[1,1,0]
	v_pk_add_f32 v[120:121], v[122:123], v[120:121]
	v_pk_add_f32 v[54:55], v[54:55], v[54:55] op_sel:[0,1] op_sel_hi:[1,0]
	v_pk_mul_f32 v[110:111], v[62:63], v[110:111]
	v_and_b32_e32 v69, 0xffff0000, v57
	v_and_b32_e32 v68, 0xffff0000, v56
	v_mov_b32_e32 v125, v129
	v_mov_b32_e32 v127, v130
	v_mov_b32_e32 v55, v128
	v_mov_b32_e32 v121, v111
	v_lshlrev_b32_e32 v67, 16, v57
	v_lshlrev_b32_e32 v66, 16, v56
	v_pk_mul_f32 v[112:113], v[68:69], v[68:69]
	v_pk_add_f32 v[122:123], v[124:125], v[126:127]
	v_pk_add_f32 v[54:55], v[120:121], v[54:55]
	v_pk_fma_f32 v[112:113], v[66:67], v[66:67], v[112:113]
	v_pk_add_f32 v[54:55], v[54:55], v[122:123]
	v_lshlrev_b32_e32 v57, 16, v59
	v_lshlrev_b32_e32 v56, 16, v58
	v_and_b32_e32 v59, 0xffff0000, v59
	v_and_b32_e32 v58, 0xffff0000, v58
	v_pk_add_f32 v[112:113], v[112:113], v[112:113] op_sel:[0,1] op_sel_hi:[1,0]
	v_pk_add_f32 v[54:55], v[54:55], v[54:55] op_sel:[0,1] op_sel_hi:[1,0]
	v_pk_mul_f32 v[118:119], v[58:59], v[58:59]
	v_mov_b32_e32 v32, v54
	v_mov_b32_e32 v110, v112
	v_mov_b32_e32 v111, v33
	v_pk_fma_f32 v[118:119], v[56:57], v[56:57], v[118:119]
	v_pk_add_f32 v[54:55], v[54:55], v[112:113]
	v_pk_mul_f32 v[110:111], v[32:33], v[110:111]
	v_mul_f32_e32 v131, v31, v31
	v_mov_b32_e32 v55, v111
	v_pk_add_f32 v[110:111], v[118:119], v[118:119] op_sel:[0,1] op_sel_hi:[1,0]
	v_mul_f32_e32 v30, v51, v51
	v_mov_b32_e32 v111, v131
	v_lshlrev_b32_e32 v44, 16, v45
	v_and_b32_e32 v45, 0xffff0000, v45
	v_pk_add_f32 v[54:55], v[54:55], v[110:111]
	v_pk_fma_f32 v[110:111], v[50:51], v[50:51], v[30:31] op_sel_hi:[1,1,0]
	v_mul_f32_e32 v30, v53, v53
	v_mul_f32_e32 v60, v44, v44
	v_mul_f32_e32 v62, v45, v45
	v_pk_fma_f32 v[112:113], v[52:53], v[52:53], v[30:31] op_sel_hi:[1,1,0]
	v_mov_b32_e32 v111, v60
	v_mov_b32_e32 v113, v62
	v_pk_add_f32 v[110:111], v[110:111], v[112:113]
	v_lshlrev_b32_e32 v62, 1, v34
	v_pk_add_f32 v[54:55], v[54:55], v[110:111]
	ds_read_b128 v[110:113], v78
	v_add_f32_e32 v30, v54, v55
	s_nop 1
	v_add_f32_dpp v30, v30, v30 quad_perm:[1,0,3,2] row_mask:0xf bank_mask:0xf bound_ctrl:1
	s_nop 1
	v_add_f32_dpp v30, v30, v30 quad_perm:[2,3,0,1] row_mask:0xf bank_mask:0xf bound_ctrl:1
	s_nop 1
	v_add_f32_dpp v30, v30, v30 row_ror:4 row_mask:0xf bank_mask:0xf bound_ctrl:1
	s_nop 1
	v_add_f32_dpp v30, v30, v30 row_ror:8 row_mask:0xf bank_mask:0xf bound_ctrl:1
	s_nop 0
	v_readlane_b32 s20, v30, 16
	v_readlane_b32 s21, v30, 48
	v_readlane_b32 s2, v30, 0
	v_readlane_b32 s3, v30, 32
	v_mov_b32_e32 v54, s20
	v_mov_b32_e32 v55, s21
	v_pk_add_f32 v[54:55], s[2:3], v[54:55]
	s_lshl_b64 s[2:3], s[90:91], 12
	v_add_f32_e32 v30, v54, v55
	v_fmamk_f32 v30, v30, 0x3a000000, v106
	v_rsq_f32_e32 v54, v30
	s_add_u32 s20, s84, s2
	s_addc_u32 s21, s26, s3
	s_and_b64 vcc, exec, s[18:19]
	v_pk_mul_f32 v[116:117], v[54:55], v[116:117] op_sel_hi:[0,1]
	v_pk_mul_f32 v[114:115], v[54:55], v[114:115] op_sel_hi:[0,1]
	s_waitcnt vmcnt(7) lgkmcnt(0)
	v_pk_fma_f32 v[46:47], v[110:111], v[114:115], v[46:47]
	v_pk_fma_f32 v[48:49], v[112:113], v[116:117], v[48:49]
	s_cbranch_vccz .LBB0_792
	v_cvt_pk_bf16_f32 v110, v46, v47
	v_cvt_pk_bf16_f32 v111, v48, v49
	global_store_dwordx2 v62, v[110:111], s[20:21]

; __device__ __forceinline__ f32x4 ld_bf4(const bf16_t* p) { const u32x2 w = *(const u32x2*)p; return (f32x4){__builtin_bit_cast(float, w.x << 16), __builtin_bit_cast(float, w.x & 0xffff0000u), __builtin_bit_cast(float, w.y << 16), __builtin_bit_cast(float, w.y & 0xffff0000u)}; }
; template <bool FAST>
; __device__ __forceinline__ void p7_route_t(Frame& F, const bool do_route) {
;     ...
;         const int row_ = FAST ? (F.bx * NIT + it) * 8 + F.wave : gw + it * NGW;
;         const bool valid = row_ < M_LAT; const int row = valid ? row_ : M_LAT - 1;
;         const float* mr = mod + (row / T) * NMOD;
;         f32x4 v[8], xv[8]; float ss = 0.f;
; #pragma unroll
;         for (int j = 0; j < 8; ++j) { v[j] = ld_bf4(MIX + (size_t)row * D + 4 * F.lane + 256 * j); xv[j] = *(const f32x4*)(IN_X + (size_t)row * D + 4 * F.lane + 256 * j); }
;     ...
;         __syncthreads();
;         if (F.tid < 256) { const int r = F.tid >> 5; float s = IN_BROUTER[re];
; #pragma unroll 16
;             for (int j = 0; j < 32; ++j) s += part[(j * 8 + r) * 32 + re];
;             lgb[r * 32 + re] = s; }
.LBB0_828:
	s_or_b64 exec, exec, s[2:3]
	s_and_saveexec_b64 s[98:99], s[8:9]
	global_load_dword v238, v[40:41], off
	s_mov_b64 exec, s[98:99]
	s_add_i32 s16, s90, 8
	s_min_i32 s16, s16, 0x3fff
	s_ashr_i32 s17, s16, 31
	s_lshl_b64 s[100:101], s[16:17], 12
	v_lshl_add_u64 v[170:171], v[36:37], 0, s[100:101]
	global_load_dwordx2 v[122:123], v[170:171], off offset:1536
	global_load_dwordx2 v[124:125], v[170:171], off offset:3584
	global_load_dwordx2 v[126:127], v[170:171], off
	global_load_dwordx2 v[128:129], v[170:171], off offset:512
	global_load_dwordx2 v[130:131], v[170:171], off offset:1024
	global_load_dwordx2 v[132:133], v[170:171], off offset:2048
	global_load_dwordx2 v[134:135], v[170:171], off offset:2560
	global_load_dwordx2 v[136:137], v[170:171], off offset:3072
	s_lshl_b64 s[100:101], s[16:17], 13
	v_lshl_add_u64 v[170:171], v[38:39], 0, s[100:101]
	global_load_dwordx4 v[138:141], v[170:171], off
	global_load_dwordx4 v[142:145], v[170:171], off offset:1024
	global_load_dwordx4 v[146:149], v[170:171], off offset:2048
	global_load_dwordx4 v[150:153], v[170:171], off offset:3072
	s_mov_b32 s100, s92
	s_mov_b32 s101, 0
	v_lshl_add_u64 v[170:171], v[170:171], 0, s[100:101]
	global_load_dwordx4 v[154:157], v[170:171], off
	global_load_dwordx4 v[158:161], v[170:171], off offset:1024
	global_load_dwordx4 v[162:165], v[170:171], off offset:2048
	global_load_dwordx4 v[166:169], v[170:171], off offset:3072
	s_waitcnt lgkmcnt(0)
	s_barrier
	s_and_saveexec_b64 s[2:3], s[8:9]
	s_cbranch_execz .LBB0_832
	s_waitcnt vmcnt(16)
	v_mov_b32_e32 v2, v238
	s_mov_b32 s16, 0
.LBB0_830:
	v_add_u32_e32 v3, s16, v105
	v_add_u32_e32 v4, 0x10400, v3
	v_add_u32_e32 v5, 0x10800, v3
	v_add_u32_e32 v6, 0x10c00, v3
	v_add_u32_e32 v7, 0x11000, v3
	v_add_u32_e32 v8, 0x11400, v3
	v_add_u32_e32 v9, 0x11800, v3
	v_add_u32_e32 v10, 0x11c00, v3
	v_add_u32_e32 v11, 0x12000, v3
	v_add_u32_e32 v12, 0x12400, v3
	v_add_u32_e32 v13, 0x12800, v3
	v_add_u32_e32 v14, 0x12c00, v3
	v_add_u32_e32 v15, 0x13000, v3
	v_add_u32_e32 v16, 0x13400, v3
	v_add_u32_e32 v17, 0x13800, v3
	v_add_u32_e32 v18, 0x13c00, v3
	v_add_u32_e32 v3, 0x14000, v3
	ds_read_b32 v4, v4
	ds_read_b32 v5, v5
	ds_read_b32 v6, v6
	ds_read_b32 v7, v7
	ds_read_b32 v8, v8
	ds_read_b32 v9, v9
	ds_read_b32 v10, v10
	ds_read_b32 v11, v11
	ds_read_b32 v12, v12
	ds_read_b32 v13, v13
	ds_read_b32 v14, v14
	ds_read_b32 v15, v15
	ds_read_b32 v16, v16
	ds_read_b32 v17, v17
	ds_read_b32 v18, v18
	ds_read_b32 v3, v3
	s_waitcnt lgkmcnt(14)
	v_add_f32_e32 v2, v2, v4
	v_add_f32_e32 v2, v2, v5
	s_waitcnt lgkmcnt(13)
	v_add_f32_e32 v2, v2, v6
	s_waitcnt lgkmcnt(12)
	v_add_f32_e32 v2, v2, v7
	s_waitcnt lgkmcnt(11)
	v_add_f32_e32 v2, v2, v8
	s_waitcnt lgkmcnt(10)
	v_add_f32_e32 v2, v2, v9
	s_waitcnt lgkmcnt(9)
	v_add_f32_e32 v2, v2, v10
	s_waitcnt lgkmcnt(8)
	v_add_f32_e32 v2, v2, v11
	s_waitcnt lgkmcnt(7)
	v_add_f32_e32 v2, v2, v12
	s_waitcnt lgkmcnt(6)
	v_add_f32_e32 v2, v2, v13
	s_waitcnt lgkmcnt(5)
	v_add_f32_e32 v2, v2, v14
	s_waitcnt lgkmcnt(4)
	v_add_f32_e32 v2, v2, v15
	s_waitcnt lgkmcnt(3)
	v_add_f32_e32 v2, v2, v16
	s_waitcnt lgkmcnt(2)
	v_add_f32_e32 v2, v2, v17
	s_addk_i32 s16, 0x4000
	s_waitcnt lgkmcnt(1)
	v_add_f32_e32 v2, v2, v18
	s_cmpk_eq_u32 s16, 0x8000
	s_waitcnt lgkmcnt(0)
	v_add_f32_e32 v2, v2, v3
	s_cbranch_scc0 .LBB0_830
	ds_write_b32 v103, v2
